# baseline (speedup 1.0000x reference)
.LBB1_2:
	s_or_b64 exec, exec, s[8:9]
	s_ashr_i32 s9, s2, 3
	s_and_b32 s8, s2, 7
	s_and_b32 s9, s9, -8
	s_bfe_u32 s20, s3, 0x20006
	s_or_b32 s10, s9, s8
	s_lshl_b32 s2, s2, 4
	s_lshr_b32 s22, s3, 6
	v_bfe_u32 v1, v0, 5, 1
	s_and_b32 s2, s2, 0x380
	s_lshl_b32 s8, s20, 5
	s_ashr_i32 s11, s10, 31
	s_or_b32 s2, s8, s2
	s_lshl_b64 s[8:9], s[10:11], 19
	v_lshl_or_b32 v2, s22, 1, v1
	s_waitcnt lgkmcnt(0)
	s_cmpk_gt_u32 s3, 0xff
	s_cselect_b32 s44, s46, s44
	s_cselect_b32 s45, s47, s45
	v_and_b32_e32 v108, 0xff, v0
	v_lshlrev_b32_e32 v108, 2, v108
	global_load_dword v108, v108, s[44:45]
	s_add_u32 s14, s4, s8
	v_lshlrev_b32_e32 v6, 9, v2
	v_lshlrev_b32_e32 v2, 2, v2
	v_and_b32_e32 v5, 31, v0
	s_addc_u32 s15, s5, s9
	v_and_b32_e32 v2, 12, v2
	s_bfe_u32 s4, s3, 0x20007
	v_bitop3_b32 v2, v2, v5, s4 bitop3:0x36
	s_lshl_b32 s4, s22, 10
	v_lshl_or_b32 v192, v2, 4, v6
	s_add_i32 s21, s4, 0
	s_mov_b32 s4, m0
	s_mov_b32 m0, s21
	s_nop 0
	global_load_lds_dwordx4 v192, s[6:7]
	s_mov_b32 m0, s4
	s_add_u32 s4, s6, 0x2000
	s_addc_u32 s5, s7, 0
	s_add_i32 s31, s21, 0x2000
	s_mov_b32 s8, m0
	s_mov_b32 m0, s31
	s_nop 0
	global_load_lds_dwordx4 v192, s[4:5]
	s_mov_b32 m0, s8
	s_add_u32 s4, s6, 0x4000
	s_addc_u32 s5, s7, 0
	s_add_i32 s33, s21, 0x4000
	s_mov_b32 s8, m0
	s_mov_b32 m0, s33
	s_nop 0
	global_load_lds_dwordx4 v192, s[4:5]
	s_mov_b32 m0, s8
	s_add_u32 s4, s6, 0x6000
	s_addc_u32 s5, s7, 0
	s_add_i32 s34, s21, 0x6000
	s_mov_b32 s8, m0
	s_mov_b32 m0, s34
	s_nop 0
	global_load_lds_dwordx4 v192, s[4:5]
	s_mov_b32 m0, s8
	s_add_u32 s4, s6, 0x8000
	s_addc_u32 s5, s7, 0
	s_add_i32 s23, s21, 0x8000
	s_mov_b32 s8, m0
	s_mov_b32 m0, s23
	s_nop 0
	global_load_lds_dwordx4 v192, s[4:5]
	s_mov_b32 m0, s8
	s_add_u32 s4, s6, 0xa000
	s_addc_u32 s5, s7, 0
	s_add_i32 s24, s21, 0xa000
	s_mov_b32 s8, m0
	s_mov_b32 m0, s24
	s_nop 0
	global_load_lds_dwordx4 v192, s[4:5]
	s_mov_b32 m0, s8
	s_add_u32 s4, s6, 0xc000
	s_addc_u32 s5, s7, 0
	s_add_i32 s25, s21, 0xc000
	s_mov_b32 s8, m0
	s_mov_b32 m0, s25
	s_nop 0
	global_load_lds_dwordx4 v192, s[4:5]
	s_mov_b32 m0, s8
	s_add_u32 s4, s6, 0xe000
	s_addc_u32 s5, s7, 0
	s_add_i32 s26, s21, 0xe000
	s_mov_b32 s8, m0
	s_mov_b32 m0, s26
	s_nop 0
	global_load_lds_dwordx4 v192, s[4:5]
	s_mov_b32 m0, s8
	s_and_b32 s4, s2, 0x380
	s_lshl_b32 s4, s4, 9
	s_add_u32 s4, s14, s4
	s_addc_u32 s5, s15, 0
	s_add_i32 s27, s21, 0x10000
	s_add_i32 s28, s21, 0x12000
	s_add_i32 s29, s21, 0x14000
	s_add_i32 s30, s21, 0x16000
	s_mov_b32 s8, m0
	s_mov_b32 m0, s27
	s_nop 0
	global_load_lds_dwordx4 v192, s[4:5]
	s_mov_b32 m0, s8
	s_add_u32 s40, s4, 0x2000
	s_addc_u32 s41, s5, 0
	s_mov_b32 s8, m0
	s_mov_b32 m0, s28
	s_nop 0
	global_load_lds_dwordx4 v192, s[40:41]
	s_mov_b32 m0, s8
	s_add_u32 s40, s4, 0x4000
	s_addc_u32 s41, s5, 0
	s_mov_b32 s8, m0
	s_mov_b32 m0, s29
	s_nop 0
	global_load_lds_dwordx4 v192, s[40:41]
	s_mov_b32 m0, s8
	s_add_u32 s40, s4, 0x6000
	s_addc_u32 s41, s5, 0
	s_mov_b32 s8, m0
	s_mov_b32 m0, s30
	s_nop 0
	global_load_lds_dwordx4 v192, s[40:41]
	s_mov_b32 m0, s8
	s_add_u32 s40, s4, 0x8000
	s_addc_u32 s41, s5, 0
	s_add_i32 s42, s21, 0x18000
	s_mov_b32 s8, m0
	s_mov_b32 m0, s42
	s_nop 0
	global_load_lds_dwordx4 v192, s[40:41]
	s_mov_b32 m0, s8
	s_add_u32 s40, s4, 0xa000
	s_addc_u32 s41, s5, 0
	s_add_i32 s42, s21, 0x1a000
	s_mov_b32 s8, m0
	s_mov_b32 m0, s42
	s_nop 0
	global_load_lds_dwordx4 v192, s[40:41]
	s_mov_b32 m0, s8
	s_add_u32 s40, s4, 0xc000
	s_addc_u32 s41, s5, 0
	s_add_i32 s42, s21, 0x1c000
	s_mov_b32 s8, m0
	s_mov_b32 m0, s42
	s_nop 0
	global_load_lds_dwordx4 v192, s[40:41]
	s_mov_b32 m0, s8
	s_add_u32 s40, s4, 0xe000
	s_addc_u32 s41, s5, 0
	s_add_i32 s42, s21, 0x1e000
	s_mov_b32 s8, m0
	s_mov_b32 m0, s42
	s_nop 0
	global_load_lds_dwordx4 v192, s[40:41]
	s_mov_b32 m0, s8
	s_load_dwordx2 s[8:9], s[0:1], 0x18
	s_load_dwordx2 s[12:13], s[0:1], 0x28
	v_and_b32_e32 v81, 63, v0
	v_lshlrev_b32_e32 v2, 2, v0
	v_add_u32_e32 v6, 0x22000, v2
	s_waitcnt vmcnt(16)
	ds_write_b32 v6, v108
	s_lshr_b32 s5, s3, 8
	s_lshl_b32 s16, s20, 12
	s_lshl_b32 s4, s5, 5
	s_add_i32 s35, s16, 0
	s_add_u32 s18, s6, 0x18000
	v_and_b32_e32 v2, 12, v2
	v_bfe_u32 v0, v0, 2, 2
	s_addc_u32 s19, s7, 0
	v_bitop3_b32 v0, v2, v1, v0 bitop3:0x36
	s_add_u32 s16, s14, 0x8000
	v_lshlrev_b32_e32 v100, 4, v0
	v_or_b32_e32 v0, s4, v5
	s_addc_u32 s17, s15, 0
	s_lshl_b32 s36, s5, 7
	v_lshl_add_u32 v101, v0, 9, 0
	v_lshl_or_b32 v0, v1, 4, s36
	v_add_u32_e32 v0, 0, v0
	v_add_u32_e32 v83, v101, v100
	s_waitcnt vmcnt(0)
	s_waitcnt lgkmcnt(0)
	s_barrier
	s_lshl_b32 s40, s20, 14
	s_add_i32 s40, s40, 0x10000
	v_lshl_add_u32 v108, v5, 9, s40
	v_add_u32_e32 v109, v108, v100
	ds_read_b128 v[68:71], v109
	ds_read_b128 v[76:79], v109 offset:256
	v_xor_b32_e32 v109, 0x20, v100
	v_add_u32_e32 v109, v108, v109
	ds_read_b128 v[60:63], v109
	ds_read_b128 v[72:75], v109 offset:256
	v_xor_b32_e32 v109, 0x40, v100
	v_add_u32_e32 v109, v108, v109
	ds_read_b128 v[52:55], v109
	ds_read_b128 v[64:67], v109 offset:256
	v_xor_b32_e32 v109, 0x60, v100
	v_add_u32_e32 v109, v108, v109
	ds_read_b128 v[48:51], v109
	ds_read_b128 v[56:59], v109 offset:256
	v_xor_b32_e32 v109, 0x80, v100
	v_add_u32_e32 v109, v108, v109
	ds_read_b128 v[36:39], v109
	ds_read_b128 v[44:47], v109 offset:256
	v_xor_b32_e32 v109, 0xa0, v100
	v_add_u32_e32 v109, v108, v109
	ds_read_b128 v[28:31], v109
	ds_read_b128 v[40:43], v109 offset:256
	v_xor_b32_e32 v109, 0xc0, v100
	v_add_u32_e32 v109, v108, v109
	ds_read_b128 v[24:27], v109
	ds_read_b128 v[32:35], v109 offset:256
	v_xor_b32_e32 v109, 0xe0, v100
	v_add_u32_e32 v109, v108, v109
	ds_read_b128 v[20:23], v109
	ds_read_b128 v[16:19], v109 offset:256
	s_waitcnt lgkmcnt(0)
	s_barrier
	s_add_u32 s40, s6, 0x10000
	s_addc_u32 s41, s7, 0
	s_mov_b32 s42, m0
	s_mov_b32 m0, s27
	s_nop 0
	global_load_lds_dwordx4 v192, s[40:41]
	s_mov_b32 m0, s42
	s_add_u32 s40, s6, 0x12000
	s_addc_u32 s41, s7, 0
	s_mov_b32 s42, m0
	s_mov_b32 m0, s28
	s_nop 0
	global_load_lds_dwordx4 v192, s[40:41]
	s_mov_b32 m0, s42
	s_add_u32 s40, s6, 0x14000
	s_addc_u32 s41, s7, 0
	s_mov_b32 s42, m0
	s_mov_b32 m0, s29
	s_nop 0
	global_load_lds_dwordx4 v192, s[40:41]
	s_mov_b32 m0, s42
	s_add_u32 s40, s6, 0x16000
	s_addc_u32 s41, s7, 0
	s_mov_b32 s42, m0
	s_mov_b32 m0, s30
	s_nop 0
	global_load_lds_dwordx4 v192, s[40:41]
	s_mov_b32 m0, s42
	v_add_u32_e32 v80, 0x22000, v0
	ds_read_b128 v[84:87], v83
	ds_read_b128 v[0:3], v80
	ds_read_b128 v[4:7], v80 offset:32
	ds_read_b128 v[8:11], v80 offset:64
	ds_read_b128 v[12:15], v80 offset:96
	ds_read_b128 v[88:91], v83 offset:256
	s_waitcnt vmcnt(15) lgkmcnt(1)
	v_mfma_f32_32x32x16_bf16 v[0:15], v[84:87], v[68:71], v[0:15]
	v_xor_b32_e32 v102, 32, v100
	v_add_u32_e32 v84, v101, v102
	v_xor_b32_e32 v103, 64, v100
	v_add_u32_e32 v85, v101, v103
	v_xor_b32_e32 v104, 0x60, v100
	v_xor_b32_e32 v105, 0x80, v100
	v_xor_b32_e32 v106, 0xa0, v100
	s_waitcnt vmcnt(7) lgkmcnt(0)
	v_mfma_f32_32x32x16_bf16 v[0:15], v[88:91], v[76:79], v[0:15]
	ds_read_b128 v[86:89], v84
	ds_read_b128 v[90:93], v84 offset:256
	v_xor_b32_e32 v107, 0xe0, v100
	v_lshl_add_u32 v81, v81, 4, s35
	v_add_u32_e32 v81, 0x18000, v81
	v_lshl_add_u32 v82, s5, 11, v81
	s_add_u32 s36, s6, 0x1a000
	s_addc_u32 s37, s7, 0
	s_waitcnt lgkmcnt(1)
	v_mfma_f32_32x32x16_bf16 v[0:15], v[86:89], v[60:63], v[0:15]
	s_add_u32 s38, s6, 0x1c000
	s_addc_u32 s39, s7, 0
	s_add_u32 s6, s6, 0x1e000
	s_addc_u32 s7, s7, 0
	s_waitcnt vmcnt(6) lgkmcnt(0)
	v_mfma_f32_32x32x16_bf16 v[0:15], v[90:93], v[72:75], v[0:15]
	ds_read_b128 v[86:89], v85
	ds_read_b128 v[90:93], v85 offset:256
	s_waitcnt lgkmcnt(1)
	v_mfma_f32_32x32x16_bf16 v[0:15], v[86:89], v[52:55], v[0:15]
	v_add_u32_e32 v86, v101, v104
	v_add_u32_e32 v87, v101, v105
	s_waitcnt vmcnt(5) lgkmcnt(0)
	v_mfma_f32_32x32x16_bf16 v[0:15], v[90:93], v[64:67], v[0:15]
	ds_read_b128 v[88:91], v86
	ds_read_b128 v[92:95], v86 offset:256
	s_waitcnt lgkmcnt(1)
	v_mfma_f32_32x32x16_bf16 v[0:15], v[88:91], v[48:51], v[0:15]
	s_waitcnt vmcnt(4) lgkmcnt(0)
	v_mfma_f32_32x32x16_bf16 v[0:15], v[92:95], v[56:59], v[0:15]
	ds_read_b128 v[88:91], v87
	ds_read_b128 v[92:95], v87 offset:256
	s_waitcnt lgkmcnt(1)
	v_mfma_f32_32x32x16_bf16 v[0:15], v[88:91], v[36:39], v[0:15]
	v_add_u32_e32 v88, v101, v106
	v_add_u32_e32 v89, v101, v107
	s_waitcnt vmcnt(3) lgkmcnt(0)
	v_mfma_f32_32x32x16_bf16 v[0:15], v[92:95], v[44:47], v[0:15]
	ds_read_b128 v[90:93], v88
	ds_read_b128 v[94:97], v88 offset:256
	s_waitcnt lgkmcnt(1)
	v_mfma_f32_32x32x16_bf16 v[0:15], v[90:93], v[28:31], v[0:15]
	v_xor_b32_e32 v91, 0xc0, v100
	v_add_u32_e32 v90, v101, v91
	v_add_u32_e32 v101, 0x10000, v101
	v_add_u32_e32 v100, v101, v100
	v_add_u32_e32 v91, v101, v91
	s_waitcnt vmcnt(2) lgkmcnt(0)
	v_mfma_f32_32x32x16_bf16 v[0:15], v[94:97], v[40:43], v[0:15]
	ds_read_b128 v[92:95], v90
	ds_read_b128 v[96:99], v90 offset:256
	s_waitcnt lgkmcnt(1)
	v_mfma_f32_32x32x16_bf16 v[0:15], v[92:95], v[24:27], v[0:15]
	ds_read_b128 v[92:95], v89
	s_waitcnt vmcnt(1) lgkmcnt(1)
	v_mfma_f32_32x32x16_bf16 v[0:15], v[96:99], v[32:35], v[0:15]
	ds_read_b128 v[96:99], v89 offset:256
	s_waitcnt lgkmcnt(1)
	v_mfma_f32_32x32x16_bf16 v[0:15], v[92:95], v[20:23], v[0:15]
	s_waitcnt vmcnt(0) lgkmcnt(0)
	v_mfma_f32_32x32x16_bf16 v[0:15], v[96:99], v[16:19], v[0:15]
	s_nop 11
	v_cvt_pk_bf16_f32 v0, v0, v1
	v_cvt_pk_bf16_f32 v1, v2, v3
	v_cvt_pk_bf16_f32 v2, v4, v5
	v_cvt_pk_bf16_f32 v3, v6, v7
	v_cvt_pk_bf16_f32 v4, v8, v9
	v_cvt_pk_bf16_f32 v5, v10, v11
	v_cvt_pk_bf16_f32 v6, v12, v13
	v_cvt_pk_bf16_f32 v7, v14, v15
	ds_write_b128 v82, v[0:3]
	ds_write_b128 v82, v[4:7] offset:1024
	s_waitcnt lgkmcnt(0)
	s_barrier
	s_mov_b32 s5, m0
	s_mov_b32 m0, s21
	s_nop 0
	global_load_lds_dwordx4 v192, s[18:19]
	s_mov_b32 m0, s5
	s_nop 0
	s_mov_b32 s5, m0
	s_mov_b32 m0, s31
	s_nop 0
	global_load_lds_dwordx4 v192, s[36:37]
	s_mov_b32 m0, s5
	s_nop 0
	s_mov_b32 s5, m0
	s_mov_b32 m0, s33
	s_nop 0
	global_load_lds_dwordx4 v192, s[38:39]
	s_mov_b32 m0, s5
	s_nop 0
	s_mov_b32 s5, m0
	s_mov_b32 m0, s34
	s_nop 0
	global_load_lds_dwordx4 v192, s[6:7]
	s_mov_b32 m0, s5
	ds_read_b128 v[0:3], v80 offset:256
	ds_read2_b32 v[4:5], v80 offset0:72 offset1:73
	ds_read_b128 v[92:95], v83 offset:32768
	ds_read2_b32 v[6:7], v80 offset0:74 offset1:75
	ds_read2_b32 v[8:9], v80 offset0:80 offset1:81
	ds_read2_b32 v[10:11], v80 offset0:82 offset1:83
	ds_read2_b32 v[12:13], v80 offset0:88 offset1:89
	ds_read2_b32 v[14:15], v80 offset0:90 offset1:91
	ds_read_b128 v[96:99], v83 offset:33024
	s_waitcnt lgkmcnt(1)
	v_mfma_f32_32x32x16_bf16 v[0:15], v[92:95], v[68:71], v[0:15]
	s_add_u32 s6, s14, 0x2000
	s_addc_u32 s7, s15, 0
	s_add_u32 s18, s14, 0x4000
	s_addc_u32 s19, s15, 0
	s_add_u32 s34, s14, 0x6000
	s_addc_u32 s35, s15, 0
	s_waitcnt lgkmcnt(0)
	v_mfma_f32_32x32x16_bf16 v[0:15], v[96:99], v[76:79], v[0:15]
	ds_read_b128 v[92:95], v84 offset:32768
	ds_read_b128 v[96:99], v84 offset:33024
	s_waitcnt lgkmcnt(1)
	v_mfma_f32_32x32x16_bf16 v[0:15], v[92:95], v[60:63], v[0:15]
	s_waitcnt lgkmcnt(0)
	v_mfma_f32_32x32x16_bf16 v[0:15], v[96:99], v[72:75], v[0:15]
	ds_read_b128 v[92:95], v85 offset:32768
	ds_read_b128 v[96:99], v85 offset:33024
	s_waitcnt lgkmcnt(1)
	v_mfma_f32_32x32x16_bf16 v[0:15], v[92:95], v[52:55], v[0:15]
	s_waitcnt lgkmcnt(0)
	v_mfma_f32_32x32x16_bf16 v[0:15], v[96:99], v[64:67], v[0:15]
	ds_read_b128 v[92:95], v86 offset:32768
	ds_read_b128 v[96:99], v86 offset:33024
	s_waitcnt lgkmcnt(1)
	v_mfma_f32_32x32x16_bf16 v[0:15], v[92:95], v[48:51], v[0:15]
	s_waitcnt lgkmcnt(0)
	v_mfma_f32_32x32x16_bf16 v[0:15], v[96:99], v[56:59], v[0:15]
	ds_read_b128 v[92:95], v87 offset:32768
	ds_read_b128 v[96:99], v87 offset:33024
	s_waitcnt lgkmcnt(1)
	v_mfma_f32_32x32x16_bf16 v[0:15], v[92:95], v[36:39], v[0:15]
	s_waitcnt lgkmcnt(0)
	v_mfma_f32_32x32x16_bf16 v[0:15], v[96:99], v[44:47], v[0:15]
	ds_read_b128 v[92:95], v88 offset:32768
	ds_read_b128 v[96:99], v88 offset:33024
	s_waitcnt lgkmcnt(1)
	v_mfma_f32_32x32x16_bf16 v[0:15], v[92:95], v[28:31], v[0:15]
	s_waitcnt lgkmcnt(0)
	v_mfma_f32_32x32x16_bf16 v[0:15], v[96:99], v[40:43], v[0:15]
	ds_read_b128 v[92:95], v90 offset:32768
	ds_read_b128 v[96:99], v90 offset:33024
	s_waitcnt lgkmcnt(1)
	v_mfma_f32_32x32x16_bf16 v[0:15], v[92:95], v[24:27], v[0:15]
	ds_read_b128 v[92:95], v89 offset:32768
	s_waitcnt lgkmcnt(1)
	v_mfma_f32_32x32x16_bf16 v[0:15], v[96:99], v[32:35], v[0:15]
	ds_read_b128 v[96:99], v89 offset:33024
	ds_read_b128 v[128:131], v81
	ds_read_b128 v[132:135], v81 offset:1024
	ds_read_b128 v[136:139], v81 offset:2048
	ds_read_b128 v[140:143], v81 offset:3072
	s_waitcnt lgkmcnt(5)
	v_mfma_f32_32x32x16_bf16 v[0:15], v[92:95], v[20:23], v[0:15]
	s_waitcnt lgkmcnt(4)
	v_mfma_f32_32x32x16_bf16 v[0:15], v[96:99], v[16:19], v[0:15]
	s_nop 11
	v_cvt_pk_bf16_f32 v0, v0, v1
	v_cvt_pk_bf16_f32 v1, v2, v3
	v_cvt_pk_bf16_f32 v2, v4, v5
	v_cvt_pk_bf16_f32 v3, v6, v7
	v_cvt_pk_bf16_f32 v4, v8, v9
	v_cvt_pk_bf16_f32 v5, v10, v11
	v_cvt_pk_bf16_f32 v6, v12, v13
	v_cvt_pk_bf16_f32 v7, v14, v15
	ds_write_b128 v82, v[0:3] offset:20480
	ds_write_b128 v82, v[4:7] offset:21504
	s_waitcnt vmcnt(4) lgkmcnt(0)
	s_barrier
	s_mov_b32 s5, m0
	s_mov_b32 m0, s23
	s_nop 0
	global_load_lds_dwordx4 v192, s[14:15]
	s_mov_b32 m0, s5
	s_nop 0
	s_mov_b32 s5, m0
	s_mov_b32 m0, s24
	s_nop 0
	global_load_lds_dwordx4 v192, s[6:7]
	s_mov_b32 m0, s5
	s_add_u32 s6, s14, 0xa000
	s_mov_b32 s5, m0
	s_mov_b32 m0, s25
	s_nop 0
	global_load_lds_dwordx4 v192, s[18:19]
	s_mov_b32 m0, s5
	s_addc_u32 s7, s15, 0
	s_mov_b32 s5, m0
	s_mov_b32 m0, s26
	s_nop 0
	global_load_lds_dwordx4 v192, s[34:35]
	s_mov_b32 m0, s5
	ds_read_b128 v[0:3], v80 offset:512
	ds_read2_b32 v[4:5], v80 offset0:136 offset1:137
	ds_read_b128 v[92:95], v100
	ds_read2_b32 v[6:7], v80 offset0:138 offset1:139
	ds_read2_b32 v[8:9], v80 offset0:144 offset1:145
	ds_read2_b32 v[10:11], v80 offset0:146 offset1:147
	ds_read2_b32 v[12:13], v80 offset0:152 offset1:153
	ds_read2_b32 v[14:15], v80 offset0:154 offset1:155
	ds_read_b128 v[96:99], v100 offset:256
	s_waitcnt lgkmcnt(1)
	v_mfma_f32_32x32x16_bf16 v[0:15], v[92:95], v[68:71], v[0:15]
	v_add_u32_e32 v100, v101, v102
	s_add_u32 s18, s14, 0xc000
	s_addc_u32 s19, s15, 0
	s_add_u32 s34, s14, 0xe000
	s_addc_u32 s35, s15, 0
	s_cmpk_gt_u32 s3, 0xff
	s_waitcnt lgkmcnt(0)
	v_mfma_f32_32x32x16_bf16 v[0:15], v[96:99], v[76:79], v[0:15]
	ds_read_b128 v[92:95], v100
	ds_read_b128 v[96:99], v100 offset:256
	v_add_u32_e32 v100, v101, v103
	s_waitcnt lgkmcnt(1)
	v_mfma_f32_32x32x16_bf16 v[0:15], v[92:95], v[60:63], v[0:15]
	s_waitcnt lgkmcnt(0)
	v_mfma_f32_32x32x16_bf16 v[0:15], v[96:99], v[72:75], v[0:15]
	ds_read_b128 v[92:95], v100
	ds_read_b128 v[96:99], v100 offset:256
	v_add_u32_e32 v100, v101, v104
	s_waitcnt lgkmcnt(1)
	v_mfma_f32_32x32x16_bf16 v[0:15], v[92:95], v[52:55], v[0:15]
	s_waitcnt lgkmcnt(0)
	v_mfma_f32_32x32x16_bf16 v[0:15], v[96:99], v[64:67], v[0:15]
	ds_read_b128 v[92:95], v100
	ds_read_b128 v[96:99], v100 offset:256
	v_add_u32_e32 v100, v101, v105
	s_waitcnt lgkmcnt(1)
	v_mfma_f32_32x32x16_bf16 v[0:15], v[92:95], v[48:51], v[0:15]
	s_waitcnt lgkmcnt(0)
	v_mfma_f32_32x32x16_bf16 v[0:15], v[96:99], v[56:59], v[0:15]
	ds_read_b128 v[92:95], v100
	ds_read_b128 v[96:99], v100 offset:256
	v_add_u32_e32 v100, v101, v106
	s_waitcnt lgkmcnt(1)
	v_mfma_f32_32x32x16_bf16 v[0:15], v[92:95], v[36:39], v[0:15]
	s_waitcnt lgkmcnt(0)
	v_mfma_f32_32x32x16_bf16 v[0:15], v[96:99], v[44:47], v[0:15]
	ds_read_b128 v[92:95], v100
	ds_read_b128 v[96:99], v100 offset:256
	s_waitcnt lgkmcnt(1)
	v_mfma_f32_32x32x16_bf16 v[0:15], v[92:95], v[28:31], v[0:15]
	s_waitcnt lgkmcnt(0)
	v_mfma_f32_32x32x16_bf16 v[0:15], v[96:99], v[40:43], v[0:15]
	ds_read_b128 v[92:95], v91
	ds_read_b128 v[96:99], v91 offset:256
	v_add_u32_e32 v91, v101, v107
	s_waitcnt lgkmcnt(1)
	v_mfma_f32_32x32x16_bf16 v[0:15], v[92:95], v[24:27], v[0:15]
	ds_read_b128 v[92:95], v91
	s_waitcnt lgkmcnt(1)
	v_mfma_f32_32x32x16_bf16 v[0:15], v[96:99], v[32:35], v[0:15]
	ds_read_b128 v[96:99], v91 offset:256
	ds_read_b128 v[144:147], v81 offset:20480
	ds_read_b128 v[148:151], v81 offset:21504
	ds_read_b128 v[152:155], v81 offset:22528
	ds_read_b128 v[156:159], v81 offset:23552
	s_waitcnt lgkmcnt(5)
	v_mfma_f32_32x32x16_bf16 v[0:15], v[92:95], v[20:23], v[0:15]
	s_waitcnt lgkmcnt(4)
	v_mfma_f32_32x32x16_bf16 v[0:15], v[96:99], v[16:19], v[0:15]
	s_nop 11
	v_cvt_pk_bf16_f32 v0, v0, v1
	v_cvt_pk_bf16_f32 v1, v2, v3
	v_cvt_pk_bf16_f32 v2, v4, v5
	v_cvt_pk_bf16_f32 v3, v6, v7
	v_cvt_pk_bf16_f32 v4, v8, v9
	v_cvt_pk_bf16_f32 v5, v10, v11
	v_cvt_pk_bf16_f32 v6, v12, v13
	v_cvt_pk_bf16_f32 v7, v14, v15
	ds_write_b128 v82, v[0:3]
	ds_write_b128 v82, v[4:7] offset:1024
	s_waitcnt vmcnt(4) lgkmcnt(0)
	s_barrier
	s_mov_b32 s5, m0
	s_mov_b32 m0, s27
	s_nop 0
	global_load_lds_dwordx4 v192, s[16:17]
	s_mov_b32 m0, s5
	s_nop 0
	s_mov_b32 s5, m0
	s_mov_b32 m0, s28
	s_nop 0
	global_load_lds_dwordx4 v192, s[6:7]
	s_mov_b32 m0, s5
	s_movk_i32 s7, 0x80
	s_mov_b32 s5, m0
	s_mov_b32 m0, s29
	s_nop 0
	global_load_lds_dwordx4 v192, s[18:19]
	s_mov_b32 m0, s5
	s_movk_i32 s6, 0xc0
	s_mov_b32 s5, m0
	s_mov_b32 m0, s30
	s_nop 0
	global_load_lds_dwordx4 v192, s[34:35]
	s_mov_b32 m0, s5
	ds_read_b128 v[0:3], v80 offset:768
	ds_read2_b32 v[4:5], v80 offset0:200 offset1:201
	ds_read_b128 v[92:95], v83
	ds_read2_b32 v[6:7], v80 offset0:202 offset1:203
	ds_read2_b32 v[8:9], v80 offset0:208 offset1:209
	ds_read2_b32 v[10:11], v80 offset0:210 offset1:211
	ds_read2_b32 v[12:13], v80 offset0:216 offset1:217
	ds_read2_b32 v[14:15], v80 offset0:218 offset1:219
	ds_read_b128 v[96:99], v83 offset:256
	s_waitcnt lgkmcnt(1)
	v_mfma_f32_32x32x16_bf16 v[0:15], v[92:95], v[68:71], v[0:15]
	s_mov_b32 s5, 0x10000
	s_waitcnt lgkmcnt(0)
	v_mfma_f32_32x32x16_bf16 v[0:15], v[96:99], v[76:79], v[0:15]
	ds_read_b128 v[68:71], v84
	ds_read_b128 v[76:79], v84 offset:256
	s_waitcnt lgkmcnt(1)
	v_mfma_f32_32x32x16_bf16 v[0:15], v[68:71], v[60:63], v[0:15]
	ds_read_b128 v[60:63], v85
	ds_read_b128 v[68:71], v85 offset:256
	s_waitcnt lgkmcnt(2)
	v_mfma_f32_32x32x16_bf16 v[0:15], v[76:79], v[72:75], v[0:15]
	s_waitcnt lgkmcnt(1)
	v_mfma_f32_32x32x16_bf16 v[0:15], v[60:63], v[52:55], v[0:15]
	ds_read_b128 v[52:55], v86
	ds_read_b128 v[60:63], v86 offset:256
	s_waitcnt lgkmcnt(2)
	v_mfma_f32_32x32x16_bf16 v[0:15], v[68:71], v[64:67], v[0:15]
	s_waitcnt lgkmcnt(1)
	v_mfma_f32_32x32x16_bf16 v[0:15], v[52:55], v[48:51], v[0:15]
	ds_read_b128 v[48:51], v87
	ds_read_b128 v[52:55], v87 offset:256
	s_waitcnt lgkmcnt(2)
	v_mfma_f32_32x32x16_bf16 v[0:15], v[60:63], v[56:59], v[0:15]
	s_waitcnt lgkmcnt(1)
	v_mfma_f32_32x32x16_bf16 v[0:15], v[48:51], v[36:39], v[0:15]
	s_waitcnt lgkmcnt(0)
	v_mfma_f32_32x32x16_bf16 v[0:15], v[52:55], v[44:47], v[0:15]
	ds_read_b128 v[36:39], v88
	ds_read_b128 v[44:47], v88 offset:256
	s_waitcnt lgkmcnt(1)
	v_mfma_f32_32x32x16_bf16 v[0:15], v[36:39], v[28:31], v[0:15]
	ds_read_b128 v[28:31], v90
	ds_read_b128 v[36:39], v90 offset:256
	s_waitcnt lgkmcnt(2)
	v_mfma_f32_32x32x16_bf16 v[0:15], v[44:47], v[40:43], v[0:15]
	s_waitcnt lgkmcnt(1)
	v_mfma_f32_32x32x16_bf16 v[0:15], v[28:31], v[24:27], v[0:15]
	ds_read_b128 v[24:27], v89
	ds_read_b128 v[28:31], v89 offset:256
	ds_read_b128 v[160:163], v81
	ds_read_b128 v[164:167], v81 offset:1024
	ds_read_b128 v[168:171], v81 offset:2048
	ds_read_b128 v[172:175], v81 offset:3072
	s_waitcnt lgkmcnt(6)
	v_mfma_f32_32x32x16_bf16 v[0:15], v[36:39], v[32:35], v[0:15]
	s_waitcnt lgkmcnt(5)
	v_mfma_f32_32x32x16_bf16 v[0:15], v[24:27], v[20:23], v[0:15]
	v_mbcnt_lo_u32_b32 v20, -1, 0
	v_mbcnt_hi_u32_b32 v193, -1, v20
	v_mov_b32_e32 v194, v193
	s_waitcnt lgkmcnt(4)
	v_mfma_f32_32x32x16_bf16 v[0:15], v[28:31], v[16:19], v[0:15]
	s_nop 11
	v_cvt_pk_bf16_f32 v0, v0, v1
	v_cvt_pk_bf16_f32 v1, v2, v3
	v_cvt_pk_bf16_f32 v2, v4, v5
	v_cvt_pk_bf16_f32 v3, v6, v7
	v_cvt_pk_bf16_f32 v4, v8, v9
	v_cvt_pk_bf16_f32 v5, v10, v11
	v_cvt_pk_bf16_f32 v6, v12, v13
	v_cvt_pk_bf16_f32 v7, v14, v15
	ds_write_b128 v82, v[0:3] offset:20480
	ds_write_b128 v82, v[4:7] offset:21504
	s_waitcnt vmcnt(4) lgkmcnt(0)
	s_barrier
	ds_read_b128 v[176:179], v81 offset:20480
	ds_read_b128 v[180:183], v81 offset:21504
	ds_read_b128 v[184:187], v81 offset:22528
	ds_read_b128 v[188:191], v81 offset:23552
	s_waitcnt lgkmcnt(0)
	s_barrier
	s_nop 0
	v_and_b32_e32 v196, 31, v194
	v_ashrrev_i32_e32 v197, 5, v194
	v_lshlrev_b32_e32 v195, 2, v194
	v_bfe_u32 v198, v194, 2, 2
	s_cbranch_scc0 .LBB1_16
	v_lshl_add_u32 v0, s20, 2, v197
	v_lshlrev_b32_e32 v3, 2, v197
	v_add_u32_e32 v1, 2, v0
	v_lshlrev_b32_e32 v2, 9, v0
	v_and_b32_e32 v3, 12, v3
	v_bfe_u32 v0, v0, 2, 2
	v_bitop3_b32 v0, v0, v196, v3 bitop3:0x36
	v_lshl_or_b32 v199, v0, 4, v2
	v_lshlrev_b32_e32 v0, 2, v1
	s_bfe_u32 s18, s3, 0x10006
	v_and_b32_e32 v0, 12, v0
	v_bfe_u32 v2, v1, 2, 2
	v_bitop3_b32 v0, v0, v196, v2 bitop3:0x36
	v_lshrrev_b32_e32 v2, 3, v194
	s_lshl_b32 s16, s18, 8
	v_and_b32_e32 v2, 2, v2
	v_bfe_u32 v3, v194, 1, 1
	s_add_i32 s16, s16, 0
	v_lshlrev_b32_e32 v4, 3, v194
	v_lshl_add_u32 v5, v197, 11, s16
	v_bitop3_b32 v2, v2, v197, v3 bitop3:0x36
	v_and_or_b32 v4, v4, 8, v5
	v_lshlrev_b32_e32 v2, 4, v2
	v_lshlrev_b32_e32 v3, 6, v198
	v_lshl_add_u32 v4, v198, 9, v4
	v_or_b32_e32 v5, v2, v3
	v_add_u32_e32 v200, v4, v5
	v_bitop3_b32 v5, v2, v3, 32 bitop3:0xde
	v_add_u32_e32 v6, 0x1000, v4
	v_add_u32_e32 v201, v6, v5
	v_xor_b32_e32 v5, 64, v3
	v_bitop3_b32 v5, v2, v5, 32 bitop3:0xde
	v_add_u32_e32 v203, v6, v5
	v_xor_b32_e32 v5, 0x80, v3
	v_bitop3_b32 v7, v2, v3, 64 bitop3:0xf6
	v_bitop3_b32 v5, v2, v5, 32 bitop3:0xde
	v_add_u32_e32 v202, v4, v7
	v_bitop3_b32 v7, v2, v3, s7 bitop3:0xf6
	v_add_u32_e32 v205, v6, v5
	v_xor_b32_e32 v5, 0xc0, v3
	v_bitop3_b32 v3, v2, v3, s6 bitop3:0xf6
	s_and_b32 s6, s22, 2
	v_lshlrev_b32_e32 v1, 9, v1
	s_lshl_b32 s27, s6, 2
	s_lshl_b32 s7, s6, 8
	s_lshl_b32 s6, s6, 12
	v_lshl_or_b32 v208, v0, 4, v1
	s_lshl_b32 s19, s20, 11
	s_add_i32 s7, s7, 0
	s_add_i32 s6, s6, 0
	v_mov_b32_e32 v0, 0
	v_bitop3_b32 v2, v2, v5, 32 bitop3:0xde
	s_waitcnt vmcnt(0)
	s_add_i32 s19, s19, 0
	s_add_i32 s16, s7, 0x20000
	s_add_i32 s7, s7, 0x20100
	v_lshlrev_b32_e32 v209, 4, v194
	s_add_i32 s6, s6, 0x18000
	v_mov_b32_e32 v14, v0
	v_mov_b32_e32 v15, v0
	v_add_u32_e32 v204, v4, v7
	v_add_u32_e32 v206, v4, v3
	v_add_u32_e32 v207, v6, v2
	v_add_u32_e32 v212, s6, v209
	s_add_u32 s6, s8, 0xfff90000
	v_mov_b32_e32 v1, v0
	v_mov_b32_e32 v2, v0
	v_mov_b32_e32 v3, v0
	v_mov_b32_e32 v4, v0
	v_mov_b32_e32 v5, v0
	v_mov_b32_e32 v6, v0
	v_mov_b32_e32 v7, v0
	v_mov_b32_e32 v8, v0
	v_mov_b32_e32 v9, v0
	v_mov_b32_e32 v10, v0
	v_mov_b32_e32 v11, v0
	v_mov_b32_e32 v12, v0
	v_mov_b32_e32 v13, v0
	v_mov_b64_e32 v[62:63], v[14:15]
	v_mov_b64_e32 v[94:95], v[14:15]
	v_mov_b64_e32 v[126:127], v[14:15]
	v_mov_b64_e32 v[30:31], v[14:15]
	v_mov_b64_e32 v[46:47], v[14:15]
	v_mov_b64_e32 v[78:79], v[14:15]
	v_mov_b64_e32 v[110:111], v[14:15]
	v_add_u32_e32 v210, s16, v195
	v_add_u32_e32 v211, s7, v195
	s_addc_u32 s7, s9, -1
	s_mov_b32 s33, 1
	s_mov_b32 s31, 0x8000
	s_mov_b32 s29, 0x10000
	v_mov_b64_e32 v[60:61], v[12:13]
	v_mov_b64_e32 v[58:59], v[10:11]
	v_mov_b64_e32 v[56:57], v[8:9]
	v_mov_b64_e32 v[54:55], v[6:7]
	v_mov_b64_e32 v[52:53], v[4:5]
	v_mov_b64_e32 v[50:51], v[2:3]
	v_mov_b64_e32 v[48:49], v[0:1]
	v_mov_b64_e32 v[92:93], v[12:13]
	v_mov_b64_e32 v[90:91], v[10:11]
	v_mov_b64_e32 v[88:89], v[8:9]
	v_mov_b64_e32 v[86:87], v[6:7]
	v_mov_b64_e32 v[84:85], v[4:5]
	v_mov_b64_e32 v[82:83], v[2:3]
	v_mov_b64_e32 v[80:81], v[0:1]
	v_mov_b64_e32 v[124:125], v[12:13]
	v_mov_b64_e32 v[122:123], v[10:11]
	v_mov_b64_e32 v[120:121], v[8:9]
	v_mov_b64_e32 v[118:119], v[6:7]
	v_mov_b64_e32 v[116:117], v[4:5]
	v_mov_b64_e32 v[114:115], v[2:3]
	v_mov_b64_e32 v[112:113], v[0:1]
	v_mov_b64_e32 v[28:29], v[12:13]
	v_mov_b64_e32 v[26:27], v[10:11]
	v_mov_b64_e32 v[24:25], v[8:9]
	v_mov_b64_e32 v[22:23], v[6:7]
	v_mov_b64_e32 v[20:21], v[4:5]
	v_mov_b64_e32 v[18:19], v[2:3]
	v_mov_b64_e32 v[16:17], v[0:1]
	v_mov_b64_e32 v[44:45], v[12:13]
	v_mov_b64_e32 v[42:43], v[10:11]
	v_mov_b64_e32 v[40:41], v[8:9]
	v_mov_b64_e32 v[38:39], v[6:7]
	v_mov_b64_e32 v[36:37], v[4:5]
	v_mov_b64_e32 v[34:35], v[2:3]
	v_mov_b64_e32 v[32:33], v[0:1]
	v_mov_b64_e32 v[76:77], v[12:13]
	v_mov_b64_e32 v[74:75], v[10:11]
	v_mov_b64_e32 v[72:73], v[8:9]
	v_mov_b64_e32 v[70:71], v[6:7]
	v_mov_b64_e32 v[68:69], v[4:5]
	v_mov_b64_e32 v[66:67], v[2:3]
	v_mov_b64_e32 v[64:65], v[0:1]
	v_mov_b64_e32 v[108:109], v[12:13]
	v_mov_b64_e32 v[106:107], v[10:11]
	v_mov_b64_e32 v[104:105], v[8:9]
	v_mov_b64_e32 v[102:103], v[6:7]
	v_mov_b64_e32 v[100:101], v[4:5]
	v_mov_b64_e32 v[98:99], v[2:3]
	v_mov_b64_e32 v[96:97], v[0:1]
	s_waitcnt lgkmcnt(0)
	v_mov_b64_e32 v[128:129], v[14:15]
	v_mov_b64_e32 v[130:131], v[14:15]
	v_mov_b64_e32 v[132:133], v[14:15]
	v_mov_b64_e32 v[134:135], v[14:15]
	v_mov_b64_e32 v[136:137], v[14:15]
	v_mov_b64_e32 v[138:139], v[14:15]
	v_mov_b64_e32 v[140:141], v[14:15]
	v_mov_b64_e32 v[142:143], v[14:15]
	v_mov_b64_e32 v[144:145], v[14:15]
	v_mov_b64_e32 v[146:147], v[14:15]
	v_mov_b64_e32 v[148:149], v[14:15]
	v_mov_b64_e32 v[150:151], v[14:15]
	v_add_u32_e32 v238, s31, v200
	v_add_u32_e32 v239, s31, v201
	v_add_u32_e32 v240, s31, v202
	v_add_u32_e32 v241, s31, v203
	v_add_u32_e32 v242, s31, v204
	v_add_u32_e32 v243, s31, v205
	v_add_u32_e32 v244, s31, v206
	v_add_u32_e32 v245, s31, v207
	ds_read_b64_tr_b16 v[222:223], v238 offset:0
	ds_read_b64_tr_b16 v[224:225], v239 offset:0
	ds_read_b64_tr_b16 v[226:227], v240 offset:0
	ds_read_b64_tr_b16 v[228:229], v241 offset:0
	ds_read_b64_tr_b16 v[230:231], v242 offset:0
	ds_read_b64_tr_b16 v[232:233], v243 offset:0
	ds_read_b64_tr_b16 v[234:235], v244 offset:0
	ds_read_b64_tr_b16 v[236:237], v245 offset:0
	s_barrier

.LBB1_10:
	s_add_i32 s29, s28, 0x8000
	s_cmp_lg_u32 s28, 0x10000
	s_cselect_b32 s29, s29, 0
	s_add_i32 s36, s19, s29
	s_andn2_b32 s38, 1, s33
	s_lshl_b32 s34, s38, 4
	s_add_i32 s34, s34, s27
	s_add_i32 s34, s34, 0x20800
	v_mov_b32_e32 v154, s34
	v_lshl_add_u32 v213, s38, 14, v212
	ds_read_b64 v[154:155], v154
	ds_read_b128 v[214:217], v213
	ds_read_b128 v[218:221], v213 offset:4096
	s_mov_b32 m0, s36
	v_mfma_f32_32x32x16_bf16 v[112:127], v[136:139], v[128:131], v[112:127]
	global_load_lds_dwordx4 v199, s[16:17]
	s_add_i32 s34, s36, 0x400
	s_mov_b32 m0, s34
	v_mfma_f32_32x32x16_bf16 v[96:111], v[136:139], v[132:135], v[96:111]
	global_load_lds_dwordx4 v208, s[16:17]
	s_add_u32 s34, s16, 0x2000
	s_addc_u32 s35, s17, 0
	s_add_i32 s37, s36, 0x2000
	s_mov_b32 m0, s37
	v_mfma_f32_32x32x16_bf16 v[80:95], v[140:143], v[128:131], v[80:95]
	global_load_lds_dwordx4 v199, s[34:35]
	s_add_i32 s37, s36, 0x2400
	s_mov_b32 m0, s37
	v_mfma_f32_32x32x16_bf16 v[64:79], v[140:143], v[132:135], v[64:79]
	global_load_lds_dwordx4 v208, s[34:35]
	s_add_u32 s34, s16, 0x4000
	s_addc_u32 s35, s17, 0
	s_add_i32 s37, s36, 0x4000
	s_mov_b32 m0, s37
	v_mfma_f32_32x32x16_bf16 v[48:63], v[144:147], v[128:131], v[48:63]
	global_load_lds_dwordx4 v199, s[34:35]
	s_add_i32 s37, s36, 0x4400
	s_mov_b32 m0, s37
	v_mfma_f32_32x32x16_bf16 v[32:47], v[144:147], v[132:135], v[32:47]
	global_load_lds_dwordx4 v208, s[34:35]
	s_add_u32 s34, s16, 0x6000
	s_addc_u32 s35, s17, 0
	s_add_i32 s37, s36, 0x6000
	s_mov_b32 m0, s37
	v_mfma_f32_32x32x16_bf16 v[0:15], v[148:151], v[128:131], v[0:15]
	global_load_lds_dwordx4 v199, s[34:35]
	s_add_i32 s37, s36, 0x6400
	s_mov_b32 m0, s37
	v_mfma_f32_32x32x16_bf16 v[16:31], v[148:151], v[132:135], v[16:31]
	global_load_lds_dwordx4 v208, s[34:35]
	s_add_u32 s6, s6, 0x8000
	s_addc_u32 s7, s7, 0
	s_waitcnt lgkmcnt(2)
	v_readfirstlane_b32 s34, v154
	v_readfirstlane_b32 s35, v155
	s_cmp_eq_u32 s33, 1
	s_cbranch_scc1 .Lpv_noB
	s_cmp_eq_u32 s34, 0
	s_cbranch_scc1 .Lpv_noA
	v_lshl_add_u32 v152, s38, 10, v210
	ds_read_b32 v152, v152
	s_nop 7
	s_waitcnt lgkmcnt(0)
	v_pk_mul_f32 v[126:127], v[152:153], v[126:127] op_sel_hi:[0,1]
	v_pk_mul_f32 v[124:125], v[152:153], v[124:125] op_sel_hi:[0,1]
	v_pk_mul_f32 v[122:123], v[152:153], v[122:123] op_sel_hi:[0,1]
	v_pk_mul_f32 v[120:121], v[152:153], v[120:121] op_sel_hi:[0,1]
	v_pk_mul_f32 v[118:119], v[152:153], v[118:119] op_sel_hi:[0,1]
	v_pk_mul_f32 v[116:117], v[152:153], v[116:117] op_sel_hi:[0,1]
	v_pk_mul_f32 v[114:115], v[152:153], v[114:115] op_sel_hi:[0,1]
	v_pk_mul_f32 v[112:113], v[152:153], v[112:113] op_sel_hi:[0,1]
	v_pk_mul_f32 v[94:95], v[152:153], v[94:95] op_sel_hi:[0,1]
	v_pk_mul_f32 v[92:93], v[152:153], v[92:93] op_sel_hi:[0,1]
	v_pk_mul_f32 v[90:91], v[152:153], v[90:91] op_sel_hi:[0,1]
	v_pk_mul_f32 v[88:89], v[152:153], v[88:89] op_sel_hi:[0,1]
	v_pk_mul_f32 v[86:87], v[152:153], v[86:87] op_sel_hi:[0,1]
	v_pk_mul_f32 v[84:85], v[152:153], v[84:85] op_sel_hi:[0,1]
	v_pk_mul_f32 v[82:83], v[152:153], v[82:83] op_sel_hi:[0,1]
	v_pk_mul_f32 v[80:81], v[152:153], v[80:81] op_sel_hi:[0,1]
	v_pk_mul_f32 v[62:63], v[152:153], v[62:63] op_sel_hi:[0,1]
	v_pk_mul_f32 v[60:61], v[152:153], v[60:61] op_sel_hi:[0,1]
	v_pk_mul_f32 v[58:59], v[152:153], v[58:59] op_sel_hi:[0,1]
	v_pk_mul_f32 v[56:57], v[152:153], v[56:57] op_sel_hi:[0,1]
	v_pk_mul_f32 v[54:55], v[152:153], v[54:55] op_sel_hi:[0,1]
	v_pk_mul_f32 v[52:53], v[152:153], v[52:53] op_sel_hi:[0,1]
	v_pk_mul_f32 v[50:51], v[152:153], v[50:51] op_sel_hi:[0,1]
	v_pk_mul_f32 v[48:49], v[152:153], v[48:49] op_sel_hi:[0,1]
	v_pk_mul_f32 v[14:15], v[152:153], v[14:15] op_sel_hi:[0,1]
	v_pk_mul_f32 v[12:13], v[152:153], v[12:13] op_sel_hi:[0,1]
	v_pk_mul_f32 v[10:11], v[152:153], v[10:11] op_sel_hi:[0,1]
	v_pk_mul_f32 v[8:9], v[152:153], v[8:9] op_sel_hi:[0,1]
	v_pk_mul_f32 v[6:7], v[152:153], v[6:7] op_sel_hi:[0,1]
	v_pk_mul_f32 v[4:5], v[152:153], v[4:5] op_sel_hi:[0,1]
	v_pk_mul_f32 v[2:3], v[152:153], v[2:3] op_sel_hi:[0,1]
	v_pk_mul_f32 v[0:1], v[152:153], v[0:1] op_sel_hi:[0,1]

	.amdhsa_kernel _Z12fused_kernelPKtS0_PKfS0_S2_S2_Pf
		.amdhsa_group_segment_fixed_size 0
		.amdhsa_private_segment_fixed_size 0
		.amdhsa_kernarg_size 56
		.amdhsa_user_sgpr_count 2
		.amdhsa_user_sgpr_dispatch_ptr 0
		.amdhsa_user_sgpr_queue_ptr 0
		.amdhsa_user_sgpr_kernarg_segment_ptr 1
		.amdhsa_user_sgpr_dispatch_id 0
		.amdhsa_user_sgpr_kernarg_preload_length 0
		.amdhsa_user_sgpr_kernarg_preload_offset 0
		.amdhsa_user_sgpr_private_segment_size 0
		.amdhsa_uses_dynamic_stack 0
		.amdhsa_enable_private_segment 0
		.amdhsa_system_sgpr_workgroup_id_x 1
		.amdhsa_system_sgpr_workgroup_id_y 0
		.amdhsa_system_sgpr_workgroup_id_z 0
		.amdhsa_system_sgpr_workgroup_info 0
		.amdhsa_system_vgpr_workitem_id 0
		.amdhsa_next_free_vgpr 248
		.amdhsa_next_free_sgpr 48
		.amdhsa_accum_offset 248
		.amdhsa_reserve_vcc 1
		.amdhsa_float_round_mode_32 0
		.amdhsa_float_round_mode_16_64 0
		.amdhsa_float_denorm_mode_32 3
		.amdhsa_float_denorm_mode_16_64 3
		.amdhsa_dx10_clamp 1
		.amdhsa_ieee_mode 1
		.amdhsa_fp16_overflow 0
		.amdhsa_tg_split 0
		.amdhsa_exception_fp_ieee_invalid_op 0
		.amdhsa_exception_fp_denorm_src 0
		.amdhsa_exception_fp_ieee_div_zero 0
		.amdhsa_exception_fp_ieee_overflow 0
		.amdhsa_exception_fp_ieee_underflow 0
		.amdhsa_exception_fp_ieee_inexact 0
		.amdhsa_exception_int_div_zero 0
	.end_amdhsa_kernel

amdhsa.kernels:
  - .agpr_count:     0
    .args:
      - .actual_access:  read_only
        .address_space:  global
        .offset:         0
        .size:           8
        .value_kind:     global_buffer
      - .actual_access:  read_only
        .address_space:  global
        .offset:         8
        .size:           8
        .value_kind:     global_buffer
      - .actual_access:  read_only
        .address_space:  global
        .offset:         16
        .size:           8
        .value_kind:     global_buffer
      - .actual_access:  read_only
        .address_space:  global
        .offset:         24
        .size:           8
        .value_kind:     global_buffer
      - .actual_access:  read_only
        .address_space:  global
        .offset:         32
        .size:           8
        .value_kind:     global_buffer
      - .address_space:  global
        .offset:         40
        .size:           8
        .value_kind:     global_buffer
      - .actual_access:  write_only
        .address_space:  global
        .offset:         48
        .size:           8
        .value_kind:     global_buffer
      - .actual_access:  write_only
        .address_space:  global
        .offset:         56
        .size:           8
        .value_kind:     global_buffer
      - .actual_access:  write_only
        .address_space:  global
        .offset:         64
        .size:           8
        .value_kind:     global_buffer
    .group_segment_fixed_size: 21520
    .kernarg_segment_align: 8
    .kernarg_segment_size: 72
    .language:       OpenCL C
    .language_version:
      - 2
      - 0
    .max_flat_workgroup_size: 256
    .name:           _Z11prep_kernelPKfS0_S0_S0_S0_PtS1_PfS1_
    .private_segment_fixed_size: 0
    .sgpr_count:     20
    .sgpr_spill_count: 0
    .symbol:         _Z11prep_kernelPKfS0_S0_S0_S0_PtS1_PfS1_.kd
    .uniform_work_group_size: 1
    .uses_dynamic_stack: false
    .vgpr_count:     70
    .vgpr_spill_count: 0
    .wavefront_size: 64
  - .agpr_count:     0
    .args:
      - .address_space:  global
        .offset:         0
        .size:           8
        .value_kind:     global_buffer
      - .address_space:  global
        .offset:         8
        .size:           8
        .value_kind:     global_buffer
      - .actual_access:  read_only
        .address_space:  global
        .offset:         16
        .size:           8
        .value_kind:     global_buffer
      - .address_space:  global
        .offset:         24
        .size:           8
        .value_kind:     global_buffer
      - .actual_access:  read_only
        .address_space:  global
        .offset:         32
        .size:           8
        .value_kind:     global_buffer
      - .actual_access:  read_only
        .address_space:  global
        .offset:         40
        .size:           8
        .value_kind:     global_buffer
      - .actual_access:  write_only
        .address_space:  global
        .offset:         48
        .size:           8
        .value_kind:     global_buffer
    .group_segment_fixed_size: 0
    .kernarg_segment_align: 8
    .kernarg_segment_size: 56
    .language:       OpenCL C
    .language_version:
      - 2
      - 0
    .max_flat_workgroup_size: 512
    .name:           _Z12fused_kernelPKtS0_PKfS0_S2_S2_Pf
    .private_segment_fixed_size: 0
    .sgpr_count:     54
    .sgpr_spill_count: 0
    .symbol:         _Z12fused_kernelPKtS0_PKfS0_S2_S2_Pf.kd
    .uniform_work_group_size: 1
    .uses_dynamic_stack: false
    .vgpr_count:     248
    .vgpr_spill_count: 0
    .wavefront_size: 64
